# v50 + GQA unit prologue de-serialised: key-tile-1 K/V loads issued right after the tile-0 staging barrier (into the step-A staging registers), tile-0 exp2 block ahead of their wait
# speedup vs baseline: 1.0030x; 1.0030x over previous
.LBB0_880:
	v_add_u32_e32 v21, 32, v185
	v_and_b32_e32 v17, 0xfffff0, v185
	v_lshlrev_b32_e32 v18, 1, v185
	v_and_b32_e32 v22, 0xfffff0, v21
	v_lshlrev_b32_e32 v23, 1, v21
	v_and_b32_e32 v16, 63, v184
	v_and_or_b32 v17, v18, 8, v17
	v_and_or_b32 v22, v23, 8, v22
	v_lshrrev_b32_e32 v17, 1, v17
	v_lshrrev_b32_e32 v19, 5, v186
	v_lshrrev_b32_e32 v22, 1, v22
	v_lshlrev_b32_e32 v23, 4, v16
	v_lshrrev_b32_e32 v18, 1, v185
	v_or_b32_e32 v17, v17, v19
	v_and_b32_e32 v20, 3, v185
	v_or_b32_e32 v19, v22, v19
	v_lshlrev_b32_e32 v22, 3, v16
	v_and_b32_e32 v23, 0xc0, v23
	v_lshlrev_b32_e32 v16, 1, v16
	v_and_or_b32 v18, v18, 4, v20
	v_lshlrev_b32_e32 v20, 1, v186
	v_and_or_b32 v23, v22, 24, v23
	v_and_b32_e32 v16, 32, v16
	v_and_b32_e32 v22, 0x100, v22
	v_lshlrev_b32_e32 v17, 9, v17
	v_lshlrev_b32_e32 v18, 6, v18
	v_or3_b32 v114, v23, v16, v22
	v_and_b32_e32 v16, 48, v20
	v_or3_b32 v17, v17, v18, v16
	v_add_u32_e32 v212, 0, v17
	v_lshrrev_b32_e32 v17, 3, v212
	v_xor_b32_e32 v17, v17, v212
	v_and_b32_e32 v17, 0x100, v17
	v_xor_b32_e32 v212, v212, v17
	v_lshlrev_b32_e32 v17, 3, v17
	v_xor_b32_e32 v212, v212, v17
	v_lshlrev_b32_e32 v19, 9, v19
	v_cvt_pk_bf16_f32 v138, v176, v177
	v_cvt_pk_bf16_f32 v139, v170, v171
	v_cvt_pk_bf16_f32 v140, v164, v165
	v_cvt_pk_bf16_f32 v141, v144, v145
	v_cvt_pk_bf16_f32 v154, v142, v143
	v_cvt_pk_bf16_f32 v155, v136, v137
	v_cvt_pk_bf16_f32 v156, v134, v135
	v_cvt_pk_bf16_f32 v157, v132, v133
	v_cvt_pk_bf16_f32 v158, v130, v131
	v_cvt_pk_bf16_f32 v159, v126, v127
	v_cvt_pk_bf16_f32 v160, v124, v125
	v_cvt_pk_bf16_f32 v161, v122, v123
	v_cvt_pk_bf16_f32 v150, v120, v121
	v_cvt_pk_bf16_f32 v151, v118, v119
	v_cvt_pk_bf16_f32 v152, v116, v117
	v_cvt_pk_bf16_f32 v153, v112, v113
	v_cvt_pk_bf16_f32 v146, v108, v109
	v_cvt_pk_bf16_f32 v147, v110, v111
	v_cvt_pk_bf16_f32 v148, v104, v105
	v_cvt_pk_bf16_f32 v149, v106, v107
	v_cvt_pk_bf16_f32 v142, v100, v101
	v_cvt_pk_bf16_f32 v143, v102, v103
	v_cvt_pk_bf16_f32 v144, v96, v97
	v_cvt_pk_bf16_f32 v145, v98, v99
	v_cvt_pk_bf16_f32 v134, v92, v93
	v_cvt_pk_bf16_f32 v135, v94, v95
	v_cvt_pk_bf16_f32 v136, v88, v89
	v_cvt_pk_bf16_f32 v137, v90, v91
	v_cvt_pk_bf16_f32 v130, v84, v85
	v_cvt_pk_bf16_f32 v131, v86, v87
	v_cvt_pk_bf16_f32 v132, v80, v81
	v_cvt_pk_bf16_f32 v133, v82, v83
	s_waitcnt vmcnt(0)
	ds_write_b128 v212, v[8:11]
	v_lshlrev_b32_e32 v8, 8, v185
	v_and_b32_e32 v9, 0x70, v184
	v_or3_b32 v16, v19, v18, v16
	v_bitop3_b32 v8, v20, v8, v9 bitop3:0xde
	v_add_u32_e32 v213, 0, v16
	v_lshrrev_b32_e32 v16, 3, v213
	v_xor_b32_e32 v16, v16, v213
	v_and_b32_e32 v16, 0x100, v16
	v_xor_b32_e32 v213, v213, v16
	v_lshlrev_b32_e32 v16, 3, v16
	v_xor_b32_e32 v213, v213, v16
	v_add_u32_e32 v214, 0, v8
	ds_write_b128 v213, v[12:15]
	ds_write_b128 v214, v[4:7] offset:32768
	v_lshlrev_b32_e32 v4, 8, v21
	v_bitop3_b32 v4, v20, v4, v9 bitop3:0xde
	v_add_u32_e32 v215, 0, v4
	ds_write_b128 v215, v[0:3] offset:32768
	v_lshlrev_b32_e32 v0, 4, v163
	v_lshlrev_b32_e32 v56, 8, v163
	v_and_b32_e32 v57, 0x70, v0
	v_bitop3_b32 v0, v162, v56, v57 bitop3:0xde
	v_add_u32_e32 v216, 0, v0
	s_waitcnt lgkmcnt(0)
	s_barrier
	s_add_u32 s16, s10, s96
	s_addc_u32 s17, s11, s97
	s_add_u32 s18, s8, s96
	s_addc_u32 s19, s9, s97
	global_load_dwordx4 v[178:181], v128, s[16:17]
	global_load_dwordx4 v[182:185], v198, s[16:17]
	global_load_dwordx4 v[186:189], v128, s[18:19]
	global_load_dwordx4 v[190:193], v198, s[18:19]
	ds_read_b128 v[16:19], v216 offset:32768
	ds_read_b128 v[20:23], v216 offset:40960
	s_waitcnt lgkmcnt(1)
	v_mfma_f32_32x32x16_bf16 v[32:47], v[16:19], v[138:141], 0
	v_or_b32_e32 v48, 32, v162
	v_bitop3_b32 v48, v48, v56, v57 bitop3:0xde
	v_add_u32_e32 v218, 0, v48
	ds_read_b128 v[48:51], v218 offset:32768
	ds_read_b128 v[52:55], v218 offset:40960
	s_cmp_lg_u32 0, -1
	s_cselect_b32 s53, 0, 0
	s_add_u32 s16, s10, s96
	s_waitcnt lgkmcnt(2)
	v_mfma_f32_32x32x16_bf16 v[16:31], v[20:23], v[138:141], 0
	s_addc_u32 s17, s11, s97
	v_mov_b32_e32 v199, v129
	s_add_u32 s18, s8, s96
	s_addc_u32 s19, s9, s97
	s_add_u32 s2, s16, s96
	s_addc_u32 s3, s17, s97
	s_waitcnt lgkmcnt(1)
	v_mfma_f32_32x32x16_bf16 v[32:47], v[48:51], v[154:157], v[32:47]
	v_or_b32_e32 v48, 64, v162
	v_bitop3_b32 v48, v48, v56, v57 bitop3:0xde
	v_add_u32_e32 v219, 0, v48
	v_lshl_add_u64 v[64:65], s[2:3], 0, v[128:129]
	s_mov_b32 s72, s73
	s_mov_b32 s74, s73
	s_mov_b32 s75, s73
	s_waitcnt lgkmcnt(0)
	v_mfma_f32_32x32x16_bf16 v[16:31], v[52:55], v[154:157], v[16:31]
	ds_read_b128 v[48:51], v219 offset:32768
	ds_read_b128 v[52:55], v219 offset:40960
	s_mov_b32 s76, s73
	s_mov_b32 s77, s73
	s_mov_b32 s78, s73
	s_mov_b32 s79, s73
	s_mov_b32 s80, s73
	s_mov_b32 s81, s73
	s_waitcnt lgkmcnt(1)
	v_mfma_f32_32x32x16_bf16 v[32:47], v[48:51], v[158:161], v[32:47]
	v_or_b32_e32 v48, 0x60, v162
	v_bitop3_b32 v48, v48, v56, v57 bitop3:0xde
	v_add_u32_e32 v220, 0, v48
	s_mov_b32 s82, s73
	s_mov_b32 s83, s73
	s_mov_b32 s84, s73
	s_mov_b32 s85, s73
	s_waitcnt lgkmcnt(0)
	v_mfma_f32_32x32x16_bf16 v[16:31], v[52:55], v[158:161], v[16:31]
	ds_read_b128 v[48:51], v220 offset:32768
	ds_read_b128 v[52:55], v220 offset:40960
	s_mov_b32 s86, s73
	s_mov_b32 s87, s73
	v_mov_b64_e32 v[0:1], s[72:73]
	v_mov_b64_e32 v[14:15], s[86:87]
	v_add_u32_e32 v209, s53, v114
	v_mov_b64_e32 v[2:3], s[74:75]
	s_waitcnt lgkmcnt(1)
	v_mfma_f32_32x32x16_bf16 v[32:47], v[48:51], v[150:153], v[32:47]
	v_or_b32_e32 v48, 0x80, v162
	v_bitop3_b32 v48, v48, v56, v57 bitop3:0xde
	v_add_u32_e32 v221, 0, v48
	v_mov_b64_e32 v[4:5], s[76:77]
	v_mov_b64_e32 v[6:7], s[78:79]
	v_mov_b64_e32 v[8:9], s[80:81]
	v_mov_b64_e32 v[10:11], s[82:83]
	s_waitcnt lgkmcnt(0)
	v_mfma_f32_32x32x16_bf16 v[16:31], v[52:55], v[150:153], v[16:31]
	ds_read_b128 v[48:51], v221 offset:32768
	ds_read_b128 v[52:55], v221 offset:40960
	v_mov_b64_e32 v[12:13], s[84:85]
	s_mov_b32 s39, 4
	v_mov_b32_e32 v217, 0
	v_readlane_b32 s80, v255, 48
	s_movk_i32 s79, 0xff
	s_movk_i32 s84, 0xffe0
	s_waitcnt lgkmcnt(1)
	v_mfma_f32_32x32x16_bf16 v[32:47], v[48:51], v[146:149], v[32:47]
	v_or_b32_e32 v48, 0xa0, v162
	v_bitop3_b32 v48, v48, v56, v57 bitop3:0xde
	v_add_u32_e32 v222, 0, v48
	s_waitcnt lgkmcnt(0)
	v_mfma_f32_32x32x16_bf16 v[16:31], v[52:55], v[146:149], v[16:31]
	ds_read_b128 v[48:51], v222 offset:32768
	ds_read_b128 v[52:55], v222 offset:40960
	s_waitcnt lgkmcnt(1)
	v_mfma_f32_32x32x16_bf16 v[32:47], v[48:51], v[142:145], v[32:47]
	v_or_b32_e32 v48, 0xc0, v162
	v_bitop3_b32 v48, v48, v56, v57 bitop3:0xde
	v_add_u32_e32 v224, 0, v48
	s_waitcnt lgkmcnt(0)
	v_mfma_f32_32x32x16_bf16 v[16:31], v[52:55], v[142:145], v[16:31]
	ds_read_b128 v[48:51], v224 offset:32768
	ds_read_b128 v[52:55], v224 offset:40960
	s_waitcnt lgkmcnt(1)
	v_mfma_f32_32x32x16_bf16 v[32:47], v[48:51], v[134:137], v[32:47]
	v_or_b32_e32 v48, 0xe0, v162
	v_bitop3_b32 v48, v48, v56, v57 bitop3:0xde
	v_add_u32_e32 v223, 0, v48
	s_waitcnt lgkmcnt(0)
	v_mfma_f32_32x32x16_bf16 v[16:31], v[52:55], v[134:137], v[16:31]
	ds_read_b128 v[48:51], v223 offset:32768
	ds_read_b128 v[52:55], v223 offset:40960
	global_load_dwordx4 v[162:165], v[64:65], off
	v_lshl_add_u64 v[64:65], s[2:3], 0, v[198:199]
	s_waitcnt lgkmcnt(1)
	v_mfma_f32_32x32x16_bf16 v[32:47], v[48:51], v[130:133], v[32:47]
	global_load_dwordx4 v[166:169], v[64:65], off
	s_waitcnt lgkmcnt(0)
	v_mfma_f32_32x32x16_bf16 v[16:31], v[52:55], v[130:133], v[16:31]
	s_nop 8
	s_add_u32 s16, s18, s96
	s_addc_u32 s17, s19, s97
	v_lshl_add_u64 v[64:65], s[16:17], 0, v[128:129]
	global_load_dwordx4 v[170:173], v[64:65], off
	v_lshl_add_u64 v[64:65], s[16:17], 0, v[198:199]
	global_load_dwordx4 v[174:177], v[64:65], off
	s_and_b64 s[2:3], s[14:15], exec
	s_cselect_b32 s14, 3, 35
	v_exp_f32_e32 v64, v32
	v_exp_f32_e32 v65, v33
	v_exp_f32_e32 v66, v34
	v_exp_f32_e32 v67, v35
	v_exp_f32_e32 v68, v36
	v_exp_f32_e32 v69, v37
	v_exp_f32_e32 v70, v38
	v_exp_f32_e32 v71, v39
	v_exp_f32_e32 v72, v40
	v_exp_f32_e32 v73, v41
	v_exp_f32_e32 v74, v42
	v_exp_f32_e32 v80, v16
	v_exp_f32_e32 v81, v17
	v_exp_f32_e32 v75, v43
	v_exp_f32_e32 v76, v44
	v_exp_f32_e32 v77, v45
	v_exp_f32_e32 v78, v46
	v_exp_f32_e32 v79, v47
	v_exp_f32_e32 v82, v18
	v_exp_f32_e32 v83, v19
	v_lshl_add_u64 v[16:17], s[12:13], 0, v[128:129]
	v_lshl_add_u64 v[18:19], s[12:13], 0, v[198:199]
	v_exp_f32_e32 v94, v30
	v_exp_f32_e32 v95, v31
	v_exp_f32_e32 v92, v28
	v_exp_f32_e32 v93, v29
	v_exp_f32_e32 v196, v26
	v_exp_f32_e32 v197, v27
	v_exp_f32_e32 v194, v24
	v_exp_f32_e32 v195, v25
	v_exp_f32_e32 v86, v22
	v_exp_f32_e32 v87, v23
	v_exp_f32_e32 v84, v20
	v_exp_f32_e32 v85, v21
	s_addk_i32 s53, 0x4000
	v_lshl_add_u64 v[200:201], s[64:65], 0, v[16:17]
	v_lshl_add_u64 v[202:203], s[64:65], 0, v[18:19]
	v_lshl_add_u64 v[204:205], s[66:67], 0, v[16:17]
	v_lshl_add_u64 v[206:207], s[66:67], 0, v[18:19]
	v_mov_b64_e32 v[62:63], v[14:15]
	v_mov_b64_e32 v[46:47], v[14:15]
	v_mov_b64_e32 v[30:31], v[14:15]
	v_add_u32_e32 v211, s53, v114
	v_mov_b64_e32 v[60:61], v[12:13]
	v_mov_b64_e32 v[58:59], v[10:11]
	v_mov_b64_e32 v[56:57], v[8:9]
	v_mov_b64_e32 v[54:55], v[6:7]
	v_mov_b64_e32 v[52:53], v[4:5]
	v_mov_b64_e32 v[50:51], v[2:3]
	v_mov_b64_e32 v[48:49], v[0:1]
	v_mov_b64_e32 v[44:45], v[12:13]
	v_mov_b64_e32 v[42:43], v[10:11]
	v_mov_b64_e32 v[40:41], v[8:9]
	v_mov_b64_e32 v[38:39], v[6:7]
	v_mov_b64_e32 v[36:37], v[4:5]
	v_mov_b64_e32 v[34:35], v[2:3]
	v_mov_b64_e32 v[32:33], v[0:1]
	v_mov_b64_e32 v[28:29], v[12:13]
	v_mov_b64_e32 v[26:27], v[10:11]
	v_mov_b64_e32 v[24:25], v[8:9]
	v_mov_b64_e32 v[22:23], v[6:7]
	v_mov_b64_e32 v[20:21], v[4:5]
	v_mov_b64_e32 v[18:19], v[2:3]
	v_mov_b64_e32 v[16:17], v[0:1]
	s_waitcnt vmcnt(4)
	ds_write_b128 v212, v[178:181] offset:16384
	ds_write_b128 v213, v[182:185] offset:16384
	ds_write_b128 v214, v[186:189] offset:49152
	ds_write_b128 v215, v[190:193] offset:49152
	s_mov_b32 s53, 0x38e38e39
	s_waitcnt lgkmcnt(0)
	s_barrier
